# expert GEMM unit enumeration: an XCD's eight concurrent row tiles are consecutive (shared expert weight tiles in that XCD's L2) inside full 64-row-tile super-groups; last partial group unchanged
# speedup vs baseline: 1.0021x; 1.0021x over previous
.LBB0_1201:
	s_mov_b64 s[2:3], -1
	s_cmp_ge_u32 s10, s9
	s_mov_b64 s[6:7], -1
	s_cbranch_scc1 .LBB0_1200
	v_readlane_b32 s2, v255, 41
	v_readlane_b32 s6, v255, 40
	s_waitcnt lgkmcnt(0)
	s_lshr_b32 s2, s2, 16
	s_cmp_lg_u32 s2, 0
	s_cselect_b64 s[2:3], -1, 0
	s_cmp_lg_u64 s[2:3], 0
	s_addc_u32 s15, s6, s10
	s_and_b32 s13, s10, 7
	s_xor_b32 s3, s13, 7
	s_lshr_b32 s2, s10, 6
	s_add_i32 s3, s3, s8
	s_and_b32 s2, s2, 0x3fffff8
	s_ashr_i32 s6, s3, 3
	s_bfe_u32 s3, s10, 0x30003
	s_or_b32 s14, s3, s2
	s_lshr_b32 s87, s14, 3
	s_lshl_b32 s86, s87, 6
	s_lshl_b32 s88, s13, 3
	s_or_b32 s86, s86, s88
	s_and_b32 s88, s14, 7
	s_or_b32 s86, s86, s88
	s_lshl_b32 s88, s14, 3
	s_or_b32 s88, s88, s13
	s_lshr_b32 s89, s8, 6
	s_cmp_lt_u32 s87, s89
	s_cselect_b32 s86, s86, s88
	s_cmp_lt_i32 s86, s8
	s_mov_b64 s[2:3], 0
	s_cselect_b64 s[6:7], -1, 0
	s_mov_b32 s10, s15
	s_branch .LBB0_1200
.LBB0_1203:
	s_xor_b64 s[6:7], s[2:3], -1
	s_mov_b64 s[2:3], -1
	s_and_b64 vcc, exec, s[6:7]
	s_cbranch_vccz .LBB0_1198
	s_lshl_b32 s2, s14, 3
	s_mov_b32 s6, s86
	s_lshl_b32 s2, s12, 2
	s_add_i32 s2, s2, 0
	s_add_i32 s3, s2, 0x21004
	s_add_i32 s2, s12, 1
	v_and_b32_e32 v2, 63, v0
	v_lshlrev_b32_e32 v2, 2, v2
	v_add_u32_e32 v2, 0x21004, v2
	ds_read_b32 v2, v2
	s_waitcnt lgkmcnt(0)
	v_cmp_ge_i32_e64 s[84:85], s6, v2
	s_bcnt1_i32_b32 s12, s84
	s_lshl_b32 s7, s12, 2
	s_add_i32 s7, s7, 0x21000
	s_cmp_lt_u32 s11, 20
	s_cselect_b64 s[2:3], -1, 0
	s_and_b64 s[14:15], s[4:5], s[2:3]
	s_and_saveexec_b64 s[2:3], s[14:15]
	s_cbranch_execz .LBB0_1197
	s_mul_i32 s13, s11, 12
	s_add_i32 s13, s13, 0
	s_add_i32 s13, s13, 0x21400
	v_mov_b32_e32 v2, s13
	v_mov_b32_e32 v5, s12
	ds_write_b32 v2, v5
	v_mov_b32_e32 v5, s7
	ds_read_b32 v6, v5
	s_waitcnt lgkmcnt(0)
	v_readfirstlane_b32 s7, v6
	s_sub_i32 s6, s6, s7
	s_lshl_b32 s6, s6, 8
	v_mov_b32_e32 v6, s6
	ds_write_b32 v2, v6 offset:4
	ds_read_b32 v5, v5 offset:132
	s_waitcnt lgkmcnt(0)
	v_readfirstlane_b32 s6, v5
	s_nop 1
	v_mov_b32_e32 v5, s6
	ds_write_b32 v2, v5 offset:8
	s_branch .LBB0_1197

.LBB0_1234:
	s_mov_b32 s6, s18
	s_and_b32 s7, s6, 7
	s_xor_b32 s2, s7, 7
	s_add_i32 s2, s2, s15
	s_ashr_i32 s4, s2, 3
	s_lshr_b32 s2, s6, 6
	s_and_b32 s2, s2, 0x3fffff8
	s_bfe_u32 s3, s6, 0x30003
	s_add_i32 s18, s9, s18
	s_or_b32 s8, s3, s2
	s_mov_b64 s[2:3], -1
	s_lshr_b32 s87, s8, 3
	s_lshl_b32 s86, s87, 6
	s_lshl_b32 s88, s7, 3
	s_or_b32 s86, s86, s88
	s_and_b32 s88, s8, 7
	s_or_b32 s86, s86, s88
	s_lshl_b32 s88, s8, 3
	s_or_b32 s88, s88, s7
	s_lshr_b32 s89, s15, 6
	s_cmp_lt_u32 s87, s89
	s_cselect_b32 s86, s86, s88
	s_cmp_ge_i32 s86, s15
	s_mov_b64 s[4:5], -1
	s_cbranch_scc0 .LBB0_1233
	s_cmp_ge_u32 s18, s16
	s_mov_b64 s[2:3], 0
	s_cselect_b64 s[4:5], -1, 0
	s_branch .LBB0_1233

.LBB0_1238:
	s_andn2_b64 vcc, exec, s[2:3]
	v_readfirstlane_b32 s17, v0
	s_cbranch_vccnz .LBB0_1243
	s_lshl_b32 s2, s8, 3
	s_add_i32 s3, 0, 0x21004
	s_add_i32 s4, 0, 0x21000
	s_mov_b32 s8, s86
	s_mov_b32 s5, 1
	v_and_b32_e32 v2, 63, v0
	v_lshlrev_b32_e32 v2, 2, v2
	v_add_u32_e32 v2, 0x21004, v2
	ds_read_b32 v2, v2
	s_waitcnt lgkmcnt(0)
	v_cmp_ge_i32_e64 s[84:85], s8, v2
	s_bcnt1_i32_b32 s17, s84
	s_lshl_b32 s2, s17, 2
	s_add_i32 s2, s2, 0x21000
	v_mov_b32_e32 v2, v0
	s_load_dwordx2 s[2:3], s[0:1], 0xd0
	v_ashrrev_i32_e32 v6, 31, v2
	v_lshrrev_b32_e32 v6, 26, v6
	s_waitcnt vmcnt(9)
	v_lshlrev_b32_e32 v5, 4, v2
	v_add_u32_e32 v6, v2, v6
	v_bfe_i32 v2, v2, 27, 1
	v_lshrrev_b32_e32 v2, 22, v2
	s_bfe_u32 s26, s6, 0x30006
	v_add_u32_e32 v2, v5, v2
	v_and_b32_e32 v2, 0xfffffc00, v2
	s_waitcnt lgkmcnt(0)
	s_add_u32 s6, s2, 0x5a982000
	v_sub_u32_e32 v2, v5, v2
	s_addc_u32 s7, s3, 0
	s_add_i32 s4, s17, s14
	v_lshrrev_b32_e32 v5, 4, v2
	s_ashr_i32 s5, s4, 31
	v_bitop3_b32 v2, v5, v2, 32 bitop3:0x6c
	s_lshl_b32 s9, s26, 18
	s_lshl_b64 s[4:5], s[4:5], 21
	v_ashrrev_i32_e32 v5, 31, v2
	s_add_u32 s2, s2, s4
	v_lshrrev_b32_e32 v5, 26, v5
	s_addc_u32 s3, s3, s5
	v_ashrrev_i32_e32 v6, 6, v6
	v_add_u32_e32 v5, v2, v5
	s_add_u32 s2, s2, s9
	v_ashrrev_i32_e32 v7, 6, v5
	v_lshlrev_b32_e32 v6, 5, v6
	v_and_b32_e32 v5, 0xc0, v5
	s_addc_u32 s3, s3, 0
	s_waitcnt vmcnt(8)
	v_and_b32_e32 v8, 32, v6
	v_sub_u32_e32 v2, v2, v5
	s_add_u32 s4, s2, 0x26a2000
	v_lshlrev_b32_e32 v5, 2, v7
	v_and_b32_e32 v6, 0xffffffc0, v6
	v_readlane_b32 s2, v254, 4
	v_ashrrev_i16_sdwa v2, v196, sext(v2) dst_sel:DWORD dst_unused:UNUSED_PAD src0_sel:DWORD src1_sel:BYTE_0
	v_bfe_i32 v2, v2, 0, 16
	v_add3_u32 v5, s2, v5, v6
	ds_read2st64_b32 v[6:7], v5 offset1:1
	v_add_lshl_u32 v2, v8, v2, 1
	s_addc_u32 s5, s3, 0
	s_mov_b32 s19, 1
	s_waitcnt lgkmcnt(0)
	v_lshl_add_u32 v182, v6, 10, v2
	v_lshl_add_u32 v183, v7, 10, v2
	ds_read2st64_b32 v[6:7], v5 offset0:2 offset1:3
	v_mov_b32_e32 v180, s8
	s_waitcnt lgkmcnt(0)
	v_lshl_add_u32 v185, v6, 10, v2
	v_lshl_add_u32 v186, v7, 10, v2
	s_branch .LBB0_1244

.LBB0_1250:
	v_readlane_b32 s2, v255, 41
	v_readlane_b32 s12, v255, 40
	s_waitcnt lgkmcnt(0)
	s_lshr_b32 s2, s2, 16
	s_cmp_lg_u32 s2, 0
	s_cselect_b64 s[2:3], -1, 0
	s_cmp_lg_u64 s[2:3], 0
	s_addc_u32 s33, s12, s18
	s_and_b32 s34, s18, 7
	s_xor_b32 s3, s34, 7
	s_lshr_b32 s2, s18, 6
	s_add_i32 s3, s3, s15
	s_and_b32 s2, s2, 0x3fffff8
	s_ashr_i32 s12, s3, 3
	s_bfe_u32 s3, s18, 0x30003
	s_or_b32 s35, s3, s2
	s_lshr_b32 s87, s35, 3
	s_lshl_b32 s86, s87, 6
	s_lshl_b32 s88, s34, 3
	s_or_b32 s86, s86, s88
	s_and_b32 s88, s35, 7
	s_or_b32 s86, s86, s88
	s_lshl_b32 s88, s35, 3
	s_or_b32 s88, s88, s34
	s_lshr_b32 s89, s15, 6
	s_cmp_lt_u32 s87, s89
	s_cselect_b32 s86, s86, s88
	s_cmp_lt_i32 s86, s15
	s_mov_b64 s[2:3], 0
	s_cselect_b64 s[12:13], -1, 0

.LBB0_1254:
	s_mov_b32 s82, 0
	s_andn2_b64 vcc, exec, s[2:3]
	s_mov_b64 s[12:13], 0
	s_cbranch_vccz .LBB0_1259
	s_lshl_b32 s2, s35, 3
	s_mov_b32 s24, s86
	s_mov_b32 s4, s29
	s_mov_b32 s5, s28
	s_mov_b32 s3, s27
	v_and_b32_e32 v2, 63, v0
	v_lshlrev_b32_e32 v2, 2, v2
	v_add_u32_e32 v2, 0x21004, v2
	ds_read_b32 v2, v2
	s_waitcnt lgkmcnt(0)
	v_cmp_ge_i32_e64 s[84:85], s24, v2
	s_bcnt1_i32_b32 s17, s84
	s_lshl_b32 s2, s17, 2
	s_add_i32 s2, s2, 0x21000
	v_mov_b32_e32 v2, v0
	s_add_i32 s2, s17, s14
	v_ashrrev_i32_e32 v182, 31, v2
	v_lshrrev_b32_e32 v182, 26, v182
	v_lshlrev_b32_e32 v181, 4, v2
	v_add_u32_e32 v182, v2, v182
	v_bfe_i32 v2, v2, 27, 1
	v_lshrrev_b32_e32 v2, 22, v2
	v_add_u32_e32 v2, v181, v2
	v_and_b32_e32 v2, 0xfffffc00, v2
	s_bfe_u32 s25, s18, 0x30006
	v_sub_u32_e32 v2, v181, v2
	s_ashr_i32 s3, s2, 31
	v_lshrrev_b32_e32 v181, 4, v2
	s_lshl_b32 s4, s25, 18
	s_lshl_b64 s[2:3], s[2:3], 21
	v_bitop3_b32 v2, v181, v2, 32 bitop3:0x6c
	s_add_u32 s2, s22, s2
	v_ashrrev_i32_e32 v181, 31, v2
	s_addc_u32 s3, s23, s3
	v_lshrrev_b32_e32 v181, 26, v181
	s_add_u32 s4, s2, s4
	v_ashrrev_i32_e32 v182, 6, v182
	v_add_u32_e32 v181, v2, v181
	s_addc_u32 s5, s3, 0
	s_lshl_b32 s2, s19, 10
	v_ashrrev_i32_e32 v183, 6, v181
	v_lshlrev_b32_e32 v182, 5, v182
	v_and_b32_e32 v181, 0xc0, v181
	s_add_i32 s2, s2, 0
	v_and_b32_e32 v185, 32, v182
	v_sub_u32_e32 v2, v2, v181
	v_and_b32_e32 v181, 0xffffffc0, v182
	s_add_i32 s2, s2, 0x22000
	v_lshlrev_b32_e32 v182, 2, v183
	v_add3_u32 v181, s2, v181, v182
	ds_read2st64_b32 v[182:183], v181 offset1:1
	ds_read2st64_b32 v[192:193], v181 offset0:2 offset1:3
	v_ashrrev_i16_sdwa v2, v196, sext(v2) dst_sel:DWORD dst_unused:UNUSED_PAD src0_sel:DWORD src1_sel:BYTE_0
	v_bfe_i32 v2, v2, 0, 16
	v_add_lshl_u32 v2, v185, v2, 1
	s_waitcnt lgkmcnt(0)
	v_lshl_add_u32 v182, v182, 10, v2
	v_lshl_add_u32 v183, v183, 10, v2
	v_lshl_add_u32 v185, v192, 10, v2
	v_lshl_add_u32 v186, v193, 10, v2
	s_add_i32 s19, s19, 1
	s_mov_b64 s[12:13], -1
	s_mov_b64 s[6:7], s[8:9]
	s_mov_b32 s18, s33

.LBB0_1372:
	s_mov_b32 s6, s14
	s_and_b32 s7, s6, 7
	s_xor_b32 s2, s7, 7
	s_add_i32 s2, s2, s12
	s_ashr_i32 s4, s2, 3
	s_lshr_b32 s2, s6, 5
	s_and_b32 s2, s2, 0x7fffff8
	s_bfe_u32 s3, s6, 0x30003
	s_add_i32 s14, s9, s14
	s_or_b32 s10, s3, s2
	s_mov_b64 s[2:3], -1
	s_lshr_b32 s87, s10, 3
	s_lshl_b32 s86, s87, 6
	s_lshl_b32 s88, s7, 3
	s_or_b32 s86, s86, s88
	s_and_b32 s88, s10, 7
	s_or_b32 s86, s86, s88
	s_lshl_b32 s88, s10, 3
	s_or_b32 s88, s88, s7
	s_lshr_b32 s89, s12, 6
	s_cmp_lt_u32 s87, s89
	s_cselect_b32 s86, s86, s88
	s_cmp_ge_i32 s86, s12
	s_mov_b64 s[4:5], -1
	s_cbranch_scc0 .LBB0_1371
	s_cmp_ge_u32 s14, s13
	s_mov_b64 s[2:3], 0
	s_cselect_b64 s[4:5], -1, 0
	s_branch .LBB0_1371

.LBB0_1377:
	s_andn2_b64 vcc, exec, s[2:3]
	v_readfirstlane_b32 s15, v0
	s_cbranch_vccnz .LBB0_1382
	s_lshl_b32 s2, s10, 3
	s_add_i32 s3, 0, 0x21004
	s_add_i32 s4, 0, 0x21000
	s_mov_b32 s9, s86
	s_mov_b32 s5, 1
	v_and_b32_e32 v2, 63, v0
	v_lshlrev_b32_e32 v2, 2, v2
	v_add_u32_e32 v2, 0x21004, v2
	ds_read_b32 v2, v2
	s_waitcnt lgkmcnt(0)
	v_cmp_ge_i32_e64 s[84:85], s9, v2
	s_bcnt1_i32_b32 s15, s84
	s_lshl_b32 s2, s15, 2
	s_add_i32 s2, s2, 0x21000
	v_mov_b32_e32 v2, v0
	s_load_dwordx2 s[2:3], s[0:1], 0xd0
	v_ashrrev_i32_e32 v6, 31, v2
	v_lshrrev_b32_e32 v6, 26, v6
	v_lshlrev_b32_e32 v5, 4, v2
	v_add_u32_e32 v6, v2, v6
	v_bfe_i32 v2, v2, 27, 1
	v_lshrrev_b32_e32 v2, 22, v2
	v_add_u32_e32 v2, v5, v2
	s_bfe_u32 s8, s6, 0x20006
	v_and_b32_e32 v2, 0xfffffc00, v2
	v_sub_u32_e32 v2, v5, v2
	s_waitcnt lgkmcnt(0)
	s_add_u32 s4, s2, 0x52182000
	v_readlane_b32 s6, v254, 7
	v_lshrrev_b32_e32 v5, 4, v2
	s_addc_u32 s5, s3, 0
	s_lshl_b32 s6, s6, 5
	v_bitop3_b32 v2, v5, v2, 32 bitop3:0x6c
	v_readlane_b32 s7, v254, 8
	s_add_i32 s6, s15, s6
	v_ashrrev_i32_e32 v7, 31, v2
	s_ashr_i32 s7, s6, 31
	v_lshrrev_b32_e32 v7, 26, v7
	s_lshl_b32 s10, s8, 18
	s_lshl_b64 s[6:7], s[6:7], 20
	v_add_u32_e32 v7, v2, v7
	s_add_u32 s2, s2, s6
	v_lshrrev_b32_e32 v8, 6, v7
	v_and_b32_e32 v7, 0xc0, v7
	s_addc_u32 s3, s3, s7
	v_ashrrev_i32_e32 v6, 6, v6
	v_sub_u32_e32 v2, v2, v7
	s_add_u32 s2, s2, s10
	v_lshlrev_b32_e32 v5, 3, v6
	v_lshlrev_b32_e32 v6, 5, v6
	v_ashrrev_i16_sdwa v2, v196, sext(v2) dst_sel:DWORD dst_unused:UNUSED_PAD src0_sel:DWORD src1_sel:BYTE_0
	s_addc_u32 s3, s3, 0
	v_and_b32_e32 v5, 0x3ffff0, v5
	v_and_b32_e32 v6, 32, v6
	v_bfe_i32 v2, v2, 0, 16
	s_add_u32 s6, s2, 0x126a2000
	s_addc_u32 s7, s3, 0
	s_lshl_b32 s2, s9, 18
	v_add_lshl_u32 v5, v8, v5, 10
	v_add_lshl_u32 v2, v6, v2, 1
	v_add3_u32 v182, v5, s2, v2
	s_mov_b32 s16, 1
	v_add_u32_e32 v183, 0x10000, v182
	v_add_u32_e32 v184, 0x20000, v182
	v_add_u32_e32 v185, 0x30000, v182
	v_mov_b32_e32 v180, s9
	v_mov_b32_e32 v220, s8
	s_branch .LBB0_1383

.LBB0_1389:
	v_readlane_b32 s2, v255, 41
	v_readlane_b32 s10, v255, 40
	s_waitcnt lgkmcnt(0)
	s_lshr_b32 s2, s2, 16
	s_cmp_lg_u32 s2, 0
	s_cselect_b64 s[2:3], -1, 0
	s_cmp_lg_u64 s[2:3], 0
	s_addc_u32 s25, s10, s14
	s_and_b32 s26, s14, 7
	s_xor_b32 s3, s26, 7
	s_lshr_b32 s2, s14, 5
	s_add_i32 s3, s3, s12
	s_and_b32 s2, s2, 0x7fffff8
	s_ashr_i32 s10, s3, 3
	s_bfe_u32 s3, s14, 0x30003
	s_or_b32 s27, s3, s2
	s_lshr_b32 s87, s27, 3
	s_lshl_b32 s86, s87, 6
	s_lshl_b32 s88, s26, 3
	s_or_b32 s86, s86, s88
	s_and_b32 s88, s27, 7
	s_or_b32 s86, s86, s88
	s_lshl_b32 s88, s27, 3
	s_or_b32 s88, s88, s26
	s_lshr_b32 s89, s12, 6
	s_cmp_lt_u32 s87, s89
	s_cselect_b32 s86, s86, s88
	s_cmp_lt_i32 s86, s12
	s_mov_b64 s[2:3], 0
	s_cselect_b64 s[10:11], -1, 0

.LBB0_1393:
	s_mov_b32 s82, 0
	s_andn2_b64 vcc, exec, s[2:3]
	s_mov_b64 s[10:11], 0
	s_cbranch_vccz .LBB0_1398
	s_lshl_b32 s2, s27, 3
	s_mov_b32 s18, s86
	s_mov_b32 s4, s22
	s_mov_b32 s5, s21
	s_mov_b32 s3, s20
	v_and_b32_e32 v2, 63, v0
	v_lshlrev_b32_e32 v2, 2, v2
	v_add_u32_e32 v2, 0x21004, v2
	ds_read_b32 v2, v2
	s_waitcnt lgkmcnt(0)
	v_cmp_ge_i32_e64 s[84:85], s18, v2
	s_bcnt1_i32_b32 s15, s84
	s_lshl_b32 s2, s15, 2
	s_add_i32 s2, s2, 0x21000
	v_mov_b32_e32 v2, v0
	s_load_dwordx2 s[2:3], s[0:1], 0xd0
	v_ashrrev_i32_e32 v37, 31, v2
	v_lshrrev_b32_e32 v37, 26, v37
	v_lshlrev_b32_e32 v36, 4, v2
	v_add_u32_e32 v37, v2, v37
	v_bfe_i32 v2, v2, 27, 1
	v_lshrrev_b32_e32 v2, 22, v2
	v_add_u32_e32 v2, v36, v2
	v_and_b32_e32 v2, 0xfffffc00, v2
	s_bfe_u32 s19, s14, 0x20006
	s_add_i32 s16, s16, 1
	v_sub_u32_e32 v2, v36, v2
	v_lshrrev_b32_e32 v36, 4, v2
	s_waitcnt lgkmcnt(0)
	s_add_u32 s4, s2, 0x52182000
	v_bitop3_b32 v2, v36, v2, 32 bitop3:0x6c
	s_addc_u32 s5, s3, 0
	s_add_i32 s6, s15, s17
	v_ashrrev_i32_e32 v38, 31, v2
	s_ashr_i32 s7, s6, 31
	v_lshrrev_b32_e32 v38, 26, v38
	s_lshl_b32 s10, s19, 18
	s_lshl_b64 s[6:7], s[6:7], 20
	v_add_u32_e32 v38, v2, v38
	s_add_u32 s2, s2, s6
	v_lshrrev_b32_e32 v39, 6, v38
	v_and_b32_e32 v38, 0xc0, v38
	s_addc_u32 s3, s3, s7
	v_ashrrev_i32_e32 v37, 6, v37
	v_sub_u32_e32 v2, v2, v38
	s_add_u32 s2, s2, s10
	v_lshlrev_b32_e32 v36, 3, v37
	v_lshlrev_b32_e32 v37, 5, v37
	v_ashrrev_i16_sdwa v2, v196, sext(v2) dst_sel:DWORD dst_unused:UNUSED_PAD src0_sel:DWORD src1_sel:BYTE_0
	s_addc_u32 s3, s3, 0
	v_and_b32_e32 v36, 0x3ffff0, v36
	v_and_b32_e32 v37, 32, v37
	v_bfe_i32 v2, v2, 0, 16
	s_add_u32 s6, s2, 0x126a2000
	s_addc_u32 s7, s3, 0
	s_lshl_b32 s2, s18, 18
	v_add_lshl_u32 v36, v39, v36, 10
	v_add_lshl_u32 v2, v37, v2, 1
	v_add3_u32 v182, v36, s2, v2
	v_add_u32_e32 v183, 0x10000, v182
	v_add_u32_e32 v184, 0x20000, v182
	v_add_u32_e32 v185, 0x30000, v182
	s_mov_b64 s[10:11], -1
	s_mov_b32 s14, s25
